# MLA unit prologue: removed a redundant full vmcnt wait right after the first tile DMA issue
# baseline (speedup 1.0000x reference)
.LBB0_1224:
	v_mov_b32_e32 v0, v181
	v_readlane_b32 s8, v251, 6
	v_mbcnt_lo_u32_b32 v0, -1, v0
	v_mbcnt_hi_u32_b32 v203, -1, v0
	v_and_b32_e32 v205, 63, v203
	v_or_b32_e32 v0, s8, v205
	v_mul_hi_i32 v1, v0, s30
	v_lshrrev_b32_e32 v2, 31, v1
	v_ashrrev_i32_e32 v1, 2, v1
	v_add_u32_e32 v2, v1, v2
	v_mad_u64_u32 v[4:5], s[8:9], v2, s91, v[0:1]
	v_lshrrev_b32_e32 v1, 1, v2
	v_xor_b32_e32 v1, v1, v203
	v_bfi_b32 v1, -8, v4, v1
	v_cmp_lt_i32_e32 vcc, 15, v1
	v_ashrrev_i32_e32 v3, 31, v2
	v_lshlrev_b32_e32 v4, 3, v1
	s_and_saveexec_b64 s[8:9], vcc
	s_xor_b64 s[8:9], exec, s[8:9]
	v_lshlrev_b64 v[2:3], 7, v[2:3]
	v_lshl_add_u64 v[2:3], s[50:51], 0, v[2:3]
	v_add_u32_e32 v180, 0xffffff80, v4
	v_lshl_add_u64 v[16:17], v[180:181], 1, v[2:3]
	s_or_saveexec_b64 s[8:9], s[8:9]
	v_mov_b64_e32 v[18:19], 0x1000
	s_xor_b64 exec, exec, s[8:9]
	v_lshlrev_b64 v[2:3], 8, v[2:3]
	v_lshl_add_u64 v[2:3], s[48:49], 0, v[2:3]
	v_ashrrev_i32_e32 v5, 31, v4
	v_lshl_add_u64 v[16:17], v[4:5], 1, v[2:3]
	v_mov_b64_e32 v[18:19], 0x2000
	s_or_b64 exec, exec, s[8:9]
	v_add_u32_e32 v4, 0x200, v0
	v_mul_hi_i32 v1, v4, s30
	v_lshrrev_b32_e32 v2, 31, v1
	v_ashrrev_i32_e32 v1, 2, v1
	v_add_u32_e32 v2, v1, v2
	v_lshrrev_b32_e32 v1, 1, v2
	v_mad_u64_u32 v[4:5], s[8:9], v2, s91, v[4:5]
	v_xor_b32_e32 v1, v1, v203
	v_bfi_b32 v1, -8, v4, v1
	v_cmp_lt_i32_e32 vcc, 15, v1
	v_ashrrev_i32_e32 v3, 31, v2
	v_lshlrev_b32_e32 v4, 3, v1
	s_and_saveexec_b64 s[8:9], vcc
	s_xor_b64 s[8:9], exec, s[8:9]
	v_lshlrev_b64 v[2:3], 7, v[2:3]
	v_lshl_add_u64 v[2:3], s[50:51], 0, v[2:3]
	v_add_u32_e32 v180, 0xffffff80, v4
	v_lshl_add_u64 v[20:21], v[180:181], 1, v[2:3]
	s_or_saveexec_b64 s[8:9], s[8:9]
	v_mov_b64_e32 v[22:23], 0x1000
	s_xor_b64 exec, exec, s[8:9]
	v_lshlrev_b64 v[2:3], 8, v[2:3]
	v_lshl_add_u64 v[2:3], s[48:49], 0, v[2:3]
	v_ashrrev_i32_e32 v5, 31, v4
	v_lshl_add_u64 v[20:21], v[4:5], 1, v[2:3]
	v_mov_b64_e32 v[22:23], 0x2000
	s_or_b64 exec, exec, s[8:9]
	v_add_u32_e32 v2, 0x400, v0
	v_mul_hi_i32 v0, v2, s30
	v_lshrrev_b32_e32 v1, 31, v0
	v_ashrrev_i32_e32 v0, 2, v0
	v_add_u32_e32 v0, v0, v1
	v_lshrrev_b32_e32 v1, 1, v0
	v_mad_u64_u32 v[2:3], s[8:9], v0, s91, v[2:3]
	v_xor_b32_e32 v1, v1, v203
	v_bfi_b32 v2, -8, v2, v1
	v_cmp_lt_i32_e32 vcc, 15, v2
	v_ashrrev_i32_e32 v1, 31, v0
	v_lshlrev_b32_e32 v2, 3, v2
	s_and_saveexec_b64 s[8:9], vcc
	s_xor_b64 s[8:9], exec, s[8:9]
	v_lshlrev_b64 v[0:1], 7, v[0:1]
	v_lshl_add_u64 v[0:1], s[50:51], 0, v[0:1]
	v_add_u32_e32 v180, 0xffffff80, v2
	v_lshl_add_u64 v[24:25], v[180:181], 1, v[0:1]
	s_or_saveexec_b64 s[8:9], s[8:9]
	v_mov_b64_e32 v[26:27], 0x1000
	s_xor_b64 exec, exec, s[8:9]
	v_lshlrev_b64 v[0:1], 8, v[0:1]
	v_lshl_add_u64 v[0:1], s[48:49], 0, v[0:1]
	v_ashrrev_i32_e32 v3, 31, v2
	v_lshl_add_u64 v[24:25], v[2:3], 1, v[0:1]
	v_mov_b64_e32 v[26:27], 0x2000
	s_or_b64 exec, exec, s[8:9]
	s_xor_b64 s[58:59], s[4:5], -1
	s_xor_b64 s[60:61], s[6:7], -1
	s_and_b64 s[4:5], s[4:5], exec
	s_cselect_b32 s57, s79, s70
	s_lshl_b32 s21, s57, 8
	s_add_i32 s44, s21, s26
	s_add_u32 s66, s46, s44
	s_mov_b32 s4, s45
	s_mov_b32 s5, s45
	s_addc_u32 s67, s47, 0
	s_mov_b32 s6, s45
	s_mov_b32 s7, s45
	s_mov_b32 s8, s45
	s_mov_b32 s9, s45
	s_mov_b32 s10, s45
	s_mov_b32 s11, s45
	s_mov_b32 s12, s45
	s_mov_b32 s13, s45
	s_mov_b32 s14, s45
	s_mov_b32 s15, s45
	s_mov_b32 s16, s45
	s_mov_b32 s17, s45
	s_mov_b32 s18, s45
	s_mov_b32 s19, s45
	v_mov_b64_e32 v[0:1], s[4:5]
	v_mov_b64_e32 v[2:3], s[6:7]
	v_mov_b64_e32 v[4:5], s[8:9]
	v_mov_b64_e32 v[6:7], s[10:11]
	v_mov_b64_e32 v[8:9], s[12:13]
	v_mov_b64_e32 v[10:11], s[14:15]
	v_mov_b64_e32 v[12:13], s[16:17]
	v_mov_b64_e32 v[14:15], s[18:19]
	s_lshl_b64 s[4:5], s[66:67], 9
	v_readlane_b32 s6, v251, 38
	s_add_u32 s8, s6, s4
	v_readlane_b32 s4, v251, 39
	s_addc_u32 s9, s4, s5
	s_lshl_b64 s[4:5], s[66:67], 4
	v_readlane_b32 s6, v251, 43
	s_add_u32 s6, s6, s4
	v_readlane_b32 s4, v251, 45
	s_addc_u32 s7, s4, s5
	s_lshl_b64 s[4:5], s[44:45], 8
	v_readlane_b32 s10, v251, 47
	s_mov_b32 m0, s88
	s_add_u32 s4, s10, s4
	v_readlane_b32 s10, v251, 48
	s_addc_u32 s5, s10, s5
	global_load_lds_dwordx4 v[16:17], off
	v_lshlrev_b32_e32 v180, 1, v18
	s_add_i32 m0, s88, 0x2000
	v_lshrrev_b32_e32 v204, 5, v205
	v_readlane_b32 s10, v251, 63
	v_and_b32_e32 v200, 31, v203
	v_lshl_add_u64 v[126:127], v[16:17], 0, v[180:181]
	global_load_lds_dwordx4 v[20:21], off
	s_mov_b32 m0, s86
	v_or_b32_e32 v16, s10, v204
	v_lshlrev_b32_e32 v184, 1, v22
	v_mov_b32_e32 v185, v181
	global_load_lds_dwordx4 v[24:25], off
	s_mov_b32 m0, s27
	v_bitop3_b32 v18, v16, v200, 9 bitop3:0x6c
	v_and_or_b32 v16, v16, 17, s96
	v_mov_b32_e32 v17, v181
	v_lshl_add_u64 v[188:189], v[20:21], 0, v[184:185]
	v_lshlrev_b32_e32 v186, 1, v26
	v_mov_b32_e32 v187, v181
	global_load_lds_dwordx4 v[126:127], off
	s_mov_b32 m0, s38
	v_lshlrev_b64 v[16:17], 9, v[16:17]
	v_lshl_add_u64 v[120:121], v[24:25], 0, v[186:187]
	global_load_lds_dwordx4 v[188:189], off
	s_mov_b32 m0, s39
	v_lshl_add_u64 v[16:17], s[34:35], 0, v[16:17]
	v_lshlrev_b32_e32 v18, 4, v18
	v_mov_b32_e32 v19, v181
	v_readlane_b32 s10, v250, 27
	global_load_lds_dwordx4 v[120:121], off
	v_lshl_add_u64 v[16:17], v[16:17], 0, v[18:19]
	s_mov_b32 m0, s10
	v_readlane_b32 s10, v251, 57
	global_load_lds_dwordx4 v[16:17], off
	s_nop 0
	v_or_b32_e32 v16, s10, v204
	v_bitop3_b32 v18, v16, v200, 11 bitop3:0x6c
	v_and_or_b32 v16, v16, 19, s96
	v_mov_b32_e32 v17, v181
	v_lshlrev_b64 v[16:17], 9, v[16:17]
	v_lshl_add_u64 v[16:17], s[34:35], 0, v[16:17]
	v_lshlrev_b32_e32 v18, 4, v18
	v_lshl_add_u64 v[16:17], v[16:17], 0, v[18:19]
	s_mov_b32 m0, s74
	v_readlane_b32 s10, v251, 61
	global_load_lds_dwordx4 v[16:17], off
	s_nop 0
	v_or_b32_e32 v16, s10, v204
	v_bitop3_b32 v18, v16, v200, 13 bitop3:0x6c
	v_and_or_b32 v16, v16, 17, s82
	v_mov_b32_e32 v17, v181
	v_lshlrev_b64 v[16:17], 9, v[16:17]
	v_lshl_add_u64 v[16:17], s[34:35], 0, v[16:17]
	v_lshlrev_b32_e32 v18, 4, v18
	v_lshl_add_u64 v[16:17], v[16:17], 0, v[18:19]
	s_mov_b32 m0, s76
	v_readlane_b32 s10, v250, 0
	global_load_lds_dwordx4 v[16:17], off
	s_nop 0
	v_or_b32_e32 v16, s10, v204
	v_bitop3_b32 v18, v16, v200, 15 bitop3:0x6c
	v_and_or_b32 v16, v16, 19, s82
	v_mov_b32_e32 v17, v181
	v_lshlrev_b64 v[16:17], 9, v[16:17]
	v_lshl_add_u64 v[16:17], s[34:35], 0, v[16:17]
	v_lshlrev_b32_e32 v18, 4, v18
	v_lshl_add_u64 v[16:17], v[16:17], 0, v[18:19]
	s_mov_b32 m0, s78
	v_readlane_b32 s10, v250, 6
	global_load_lds_dwordx4 v[16:17], off
	s_nop 0
	v_or_b32_e32 v16, s10, v204
	v_bitop3_b32 v18, v16, v200, 9 bitop3:0x6c
	v_and_or_b32 v16, v16, 17, s84
	v_mov_b32_e32 v17, v181
	v_lshlrev_b64 v[16:17], 9, v[16:17]
	v_lshl_add_u64 v[16:17], s[34:35], 0, v[16:17]
	v_lshlrev_b32_e32 v18, 4, v18
	v_lshl_add_u64 v[16:17], v[16:17], 0, v[18:19]
	s_mov_b32 m0, s94
	v_readlane_b32 s10, v250, 9
	global_load_lds_dwordx4 v[16:17], off
	s_nop 0
	v_or_b32_e32 v16, s10, v204
	v_bitop3_b32 v18, v16, v200, 11 bitop3:0x6c
	v_and_or_b32 v16, v16, 19, s36
	v_mov_b32_e32 v17, v181
	v_lshlrev_b64 v[16:17], 9, v[16:17]
	v_lshl_add_u64 v[16:17], s[34:35], 0, v[16:17]
	v_lshlrev_b32_e32 v18, 4, v18
	v_lshl_add_u64 v[16:17], v[16:17], 0, v[18:19]
	s_mov_b32 m0, s24
	v_lshlrev_b32_e32 v20, 9, v200
	global_load_lds_dwordx4 v[16:17], off
	v_or_b32_e32 v16, s73, v204
	v_bitop3_b32 v18, v16, v200, 13 bitop3:0x6c
	v_and_or_b32 v16, v16, 17, s37
	v_mov_b32_e32 v17, v181
	v_lshlrev_b64 v[16:17], 9, v[16:17]
	v_lshl_add_u64 v[16:17], s[34:35], 0, v[16:17]
	v_lshlrev_b32_e32 v18, 4, v18
	v_lshl_add_u64 v[16:17], v[16:17], 0, v[18:19]
	s_mov_b32 m0, s28
	v_mov_b32_e32 v21, v181
	global_load_lds_dwordx4 v[16:17], off
	v_or_b32_e32 v16, s72, v204
	v_bitop3_b32 v18, v16, v200, 15 bitop3:0x6c
	v_and_or_b32 v16, v16, 19, s85
	v_mov_b32_e32 v17, v181
	v_lshlrev_b64 v[16:17], 9, v[16:17]
	v_lshl_add_u64 v[16:17], s[34:35], 0, v[16:17]
	v_lshlrev_b32_e32 v18, 4, v18
	v_lshl_add_u64 v[16:17], v[16:17], 0, v[18:19]
	s_mov_b32 m0, s90
	v_lshlrev_b32_e32 v18, 8, v204
	global_load_lds_dwordx4 v[16:17], off
	v_or_b32_e32 v16, s97, v204
	v_bitop3_b32 v26, v16, v200, 9 bitop3:0x6c
	v_and_or_b32 v16, v16, 17, s83
	v_mov_b32_e32 v17, v181
	v_lshlrev_b64 v[22:23], 9, v[16:17]
	v_lshl_add_u64 v[16:17], s[8:9], 0, v[20:21]
	v_lshl_add_u64 v[24:25], v[16:17], 0, v[18:19]
	global_load_dwordx4 v[16:19], v[24:25], off
	global_load_dwordx4 v[172:175], v[24:25], off offset:16
	v_lshl_add_u64 v[22:23], s[34:35], 0, v[22:23]
	v_lshlrev_b32_e32 v26, 4, v26
	v_mov_b32_e32 v27, v181
	v_lshl_add_u64 v[22:23], v[22:23], 0, v[26:27]
	s_mov_b32 m0, s31
	v_or_b32_e32 v21, s41, v204
	global_load_lds_dwordx4 v[22:23], off
	v_and_or_b32 v22, v21, 19, s92
	v_mov_b32_e32 v23, v181
	v_bitop3_b32 v26, v21, v200, 11 bitop3:0x6c
	v_lshlrev_b64 v[22:23], 9, v[22:23]
	v_lshl_add_u64 v[22:23], s[34:35], 0, v[22:23]
	v_lshlrev_b32_e32 v26, 4, v26
	v_lshl_add_u64 v[22:23], v[22:23], 0, v[26:27]
	s_mov_b32 m0, s42
	v_or_b32_e32 v21, s75, v204
	global_load_lds_dwordx4 v[22:23], off
	v_and_or_b32 v22, v21, 17, s93
	v_mov_b32_e32 v23, v181
	v_bitop3_b32 v26, v21, v200, 13 bitop3:0x6c
	v_lshlrev_b64 v[22:23], 9, v[22:23]
	v_lshl_add_u64 v[22:23], s[34:35], 0, v[22:23]
	v_lshlrev_b32_e32 v26, 4, v26
	v_lshl_add_u64 v[22:23], v[22:23], 0, v[26:27]
	s_mov_b32 m0, s87
	v_or_b32_e32 v21, s77, v204
	global_load_lds_dwordx4 v[22:23], off
	v_and_or_b32 v22, v21, 19, s95
	v_mov_b32_e32 v23, v181
	v_bitop3_b32 v26, v21, v200, 15 bitop3:0x6c
	v_lshlrev_b64 v[22:23], 9, v[22:23]
	v_lshl_add_u64 v[22:23], s[34:35], 0, v[22:23]
	v_lshlrev_b32_e32 v26, 4, v26
	v_lshl_add_u64 v[22:23], v[22:23], 0, v[26:27]
	s_mov_b32 m0, s71
	v_lshlrev_b32_e32 v21, 4, v200
	global_load_lds_dwordx4 v[22:23], off
	global_load_dwordx4 v[168:171], v[24:25], off offset:32
	global_load_dwordx4 v[112:115], v[24:25], off offset:48
	global_load_dwordx4 v[116:119], v[24:25], off offset:64
	global_load_dwordx4 v[122:125], v[24:25], off offset:80
	global_load_dwordx4 v[164:167], v[24:25], off offset:96
	global_load_dwordx4 v[160:163], v[24:25], off offset:112
	global_load_dwordx4 v[156:159], v[24:25], off offset:128
	global_load_dwordx4 v[152:155], v[24:25], off offset:144
	global_load_dwordx4 v[148:151], v[24:25], off offset:160
	global_load_dwordx4 v[128:131], v[24:25], off offset:176
	global_load_dwordx4 v[144:147], v[24:25], off offset:192
	global_load_dwordx4 v[140:143], v[24:25], off offset:208
	global_load_dwordx4 v[132:135], v[24:25], off offset:224
	global_load_dwordx4 v[136:139], v[24:25], off offset:240
	v_lshlrev_b32_e32 v23, 4, v204
	v_and_b32_e32 v201, 15, v203
	global_load_dwordx4 v[176:179], v21, s[6:7]
	v_or_b32_e32 v21, v23, v201
	v_add_u32_e32 v22, 0, v20
	v_lshlrev_b32_e32 v21, 4, v21
	v_add_u32_e32 v228, v22, v21
	s_waitcnt vmcnt(0)
	s_waitcnt vmcnt(0) lgkmcnt(0)
	s_barrier
	ds_read_b128 v[228:231], v228 offset:49152
	v_add_u32_e32 v28, 0x10000, v22
	v_add_u32_e32 v232, v28, v21
	ds_read_b128 v[232:235], v232
	v_add_u32_e32 v221, s43, v20
	v_add_u32_e32 v218, 0x20400, v22
	v_readlane_b32 s6, v251, 6
	s_lshl_b32 s9, s57, 2
	s_add_i32 s9, s9, 4
	v_bitop3_b32 v24, v23, v201, 1 bitop3:0x36
	v_lshlrev_b32_e32 v202, 4, v24
	v_add_u32_e32 v236, v22, v202
	ds_read_b128 v[236:239], v236 offset:49152
	v_add_u32_e32 v222, v221, v202
	s_ashr_i32 s11, s89, 31
	s_mov_b32 s10, 3
	v_add_u32_e32 v240, v28, v202
	ds_read_b128 v[240:243], v240
	ds_read_b128 v[222:225], v222
	s_waitcnt lgkmcnt(4)
	v_mfma_f32_32x32x16_bf16 v[64:79], v[228:231], v[16:19], 0
	v_bitop3_b32 v24, v23, v201, 2 bitop3:0x36
	v_lshlrev_b32_e32 v220, 4, v24
	v_add_u32_e32 v244, v22, v220
	ds_read_b128 v[244:247], v244 offset:49152
	s_waitcnt lgkmcnt(4)
	v_mfma_f32_32x32x16_bf16 v[48:63], v[232:235], v[16:19], 0
	v_add_u32_e32 v252, v28, v220
	ds_read_b128 v[252:255], v252
	s_waitcnt lgkmcnt(4)
	v_mfma_f32_32x32x16_bf16 v[64:79], v[236:239], v[172:175], v[64:79]
	v_bitop3_b32 v24, v23, v201, 3 bitop3:0x36
	v_lshlrev_b32_e32 v219, 4, v24
	v_add_u32_e32 v228, v22, v219
	ds_read_b128 v[228:231], v228 offset:49152
	s_waitcnt lgkmcnt(4)
	v_mfma_f32_32x32x16_bf16 v[48:63], v[240:243], v[172:175], v[48:63]
	v_add_u32_e32 v232, v28, v219
	ds_read_b128 v[232:235], v232
	s_waitcnt lgkmcnt(3)
	v_mfma_f32_32x32x16_bf16 v[64:79], v[244:247], v[168:171], v[64:79]
	v_bitop3_b32 v24, v23, v201, 4 bitop3:0x36
	v_lshlrev_b32_e32 v217, 4, v24
	v_add_u32_e32 v236, v22, v217
	ds_read_b128 v[236:239], v236 offset:49152
	s_waitcnt lgkmcnt(3)
	v_mfma_f32_32x32x16_bf16 v[48:63], v[252:255], v[168:171], v[48:63]
	v_add_u32_e32 v240, v28, v217
	ds_read_b128 v[240:243], v240
	s_waitcnt lgkmcnt(3)
	v_mfma_f32_32x32x16_bf16 v[64:79], v[228:231], v[112:115], v[64:79]
	v_bitop3_b32 v24, v23, v201, 5 bitop3:0x36
	v_lshlrev_b32_e32 v216, 4, v24
	v_add_u32_e32 v244, v22, v216
	ds_read_b128 v[244:247], v244 offset:49152
	s_waitcnt lgkmcnt(3)
	v_mfma_f32_32x32x16_bf16 v[48:63], v[232:235], v[112:115], v[48:63]
	v_add_u32_e32 v252, v28, v216
	ds_read_b128 v[252:255], v252
	s_waitcnt lgkmcnt(3)
	v_mfma_f32_32x32x16_bf16 v[64:79], v[236:239], v[116:119], v[64:79]
	v_bitop3_b32 v24, v23, v201, 6 bitop3:0x36
	v_lshlrev_b32_e32 v215, 4, v24
	v_add_u32_e32 v228, v22, v215
	ds_read_b128 v[228:231], v228 offset:49152
	s_waitcnt lgkmcnt(3)
	v_mfma_f32_32x32x16_bf16 v[48:63], v[240:243], v[116:119], v[48:63]
	v_add_u32_e32 v232, v28, v215
	ds_read_b128 v[232:235], v232
	s_waitcnt lgkmcnt(3)
	v_mfma_f32_32x32x16_bf16 v[64:79], v[244:247], v[122:125], v[64:79]
	v_bitop3_b32 v24, v23, v201, 7 bitop3:0x36
	v_lshlrev_b32_e32 v214, 4, v24
	v_add_u32_e32 v236, v22, v214
	ds_read_b128 v[236:239], v236 offset:49152
	s_waitcnt lgkmcnt(3)
	v_mfma_f32_32x32x16_bf16 v[48:63], v[252:255], v[122:125], v[48:63]
	v_add_u32_e32 v240, v28, v214
	ds_read_b128 v[240:243], v240
	s_waitcnt lgkmcnt(3)
	v_mfma_f32_32x32x16_bf16 v[64:79], v[228:231], v[164:167], v[64:79]
	v_bitop3_b32 v24, v23, v201, 8 bitop3:0x36
	v_lshlrev_b32_e32 v210, 4, v24
	v_add_u32_e32 v244, v22, v210
	ds_read_b128 v[244:247], v244 offset:49152
	s_waitcnt lgkmcnt(3)
	v_mfma_f32_32x32x16_bf16 v[48:63], v[232:235], v[164:167], v[48:63]
	v_add_u32_e32 v252, v28, v210
	ds_read_b128 v[252:255], v252
	s_waitcnt lgkmcnt(3)
	v_mfma_f32_32x32x16_bf16 v[64:79], v[236:239], v[160:163], v[64:79]
	v_bitop3_b32 v24, v23, v201, 9 bitop3:0x36
	v_lshlrev_b32_e32 v211, 4, v24
	v_add_u32_e32 v228, v22, v211
	ds_read_b128 v[228:231], v228 offset:49152
	s_waitcnt lgkmcnt(3)
	v_mfma_f32_32x32x16_bf16 v[48:63], v[240:243], v[160:163], v[48:63]
	v_add_u32_e32 v232, v28, v211
	ds_read_b128 v[232:235], v232
	s_waitcnt lgkmcnt(3)
	v_mfma_f32_32x32x16_bf16 v[64:79], v[244:247], v[156:159], v[64:79]
	v_bitop3_b32 v24, v23, v201, 10 bitop3:0x36
	v_lshlrev_b32_e32 v212, 4, v24
	v_add_u32_e32 v236, v22, v212
	ds_read_b128 v[236:239], v236 offset:49152
	s_waitcnt lgkmcnt(3)
	v_mfma_f32_32x32x16_bf16 v[48:63], v[252:255], v[156:159], v[48:63]
	v_add_u32_e32 v240, v28, v212
	ds_read_b128 v[240:243], v240
	s_waitcnt lgkmcnt(3)
	v_mfma_f32_32x32x16_bf16 v[64:79], v[228:231], v[152:155], v[64:79]
	v_bitop3_b32 v24, v23, v201, 11 bitop3:0x36
	v_lshlrev_b32_e32 v213, 4, v24
	v_add_u32_e32 v244, v22, v213
	ds_read_b128 v[244:247], v244 offset:49152
	s_waitcnt lgkmcnt(3)
	v_mfma_f32_32x32x16_bf16 v[48:63], v[232:235], v[152:155], v[48:63]
	v_add_u32_e32 v252, v28, v213
	ds_read_b128 v[252:255], v252
	s_waitcnt lgkmcnt(3)
	v_mfma_f32_32x32x16_bf16 v[64:79], v[236:239], v[148:151], v[64:79]
	v_bitop3_b32 v24, v23, v201, 12 bitop3:0x36
	v_lshlrev_b32_e32 v206, 4, v24
	v_add_u32_e32 v228, v22, v206
	ds_read_b128 v[228:231], v228 offset:49152
	s_waitcnt lgkmcnt(3)
	v_mfma_f32_32x32x16_bf16 v[48:63], v[240:243], v[148:151], v[48:63]
	v_add_u32_e32 v232, v28, v206
	ds_read_b128 v[232:235], v232
	s_waitcnt lgkmcnt(3)
	v_mfma_f32_32x32x16_bf16 v[64:79], v[244:247], v[128:131], v[64:79]
	v_bitop3_b32 v24, v23, v201, 13 bitop3:0x36
	v_lshlrev_b32_e32 v207, 4, v24
	v_add_u32_e32 v236, v22, v207
	ds_read_b128 v[236:239], v236 offset:49152
	s_waitcnt lgkmcnt(3)
	v_mfma_f32_32x32x16_bf16 v[48:63], v[252:255], v[128:131], v[48:63]
	v_add_u32_e32 v240, v28, v207
	ds_read_b128 v[240:243], v240
	s_waitcnt lgkmcnt(3)
	v_mfma_f32_32x32x16_bf16 v[64:79], v[228:231], v[144:147], v[64:79]
	v_bitop3_b32 v24, v23, v201, 14 bitop3:0x36
	v_lshlrev_b32_e32 v208, 4, v24
	v_add_u32_e32 v244, v22, v208
	ds_read_b128 v[244:247], v244 offset:49152
	v_bitop3_b32 v23, v23, v203, 15 bitop3:0x72
	v_lshlrev_b32_e32 v209, 4, v23
	v_add_u32_e32 v23, v22, v209
	s_waitcnt lgkmcnt(3)
	v_mfma_f32_32x32x16_bf16 v[48:63], v[232:235], v[144:147], v[48:63]
	v_add_u32_e32 v252, v28, v208
	ds_read_b128 v[252:255], v252
	s_waitcnt lgkmcnt(3)
	v_mfma_f32_32x32x16_bf16 v[64:79], v[236:239], v[140:143], v[64:79]
	ds_read_b128 v[228:231], v23 offset:49152
	v_add_u32_e32 v23, v28, v209
	v_add_u32_e32 v28, 0x18000, v22
	v_add_u32_e32 v29, v28, v213
	s_waitcnt lgkmcnt(3)
	v_mfma_f32_32x32x16_bf16 v[48:63], v[240:243], v[140:143], v[48:63]
	ds_read_b128 v[232:235], v23
	v_add_u32_e32 v23, s33, v20
	v_add_u32_e32 v20, v221, v21
	s_waitcnt lgkmcnt(3)
	v_mfma_f32_32x32x16_bf16 v[64:79], v[244:247], v[132:135], v[64:79]
	s_waitcnt lgkmcnt(2)
	v_mfma_f32_32x32x16_bf16 v[48:63], v[252:255], v[132:135], v[48:63]
	s_waitcnt lgkmcnt(1)
	v_mfma_f32_32x32x16_bf16 v[64:79], v[228:231], v[136:139], v[64:79]
	s_waitcnt lgkmcnt(0)
	v_mfma_f32_32x32x16_bf16 v[48:63], v[232:235], v[136:139], v[48:63]
	v_add_u32_e32 v236, v23, v21
	ds_read_b128 v[236:239], v236
	v_add_u32_e32 v240, v28, v21
	ds_read_b128 v[240:243], v240
	v_add_u32_e32 v244, v23, v202
	ds_read_b128 v[244:247], v244
	v_add_u32_e32 v252, v28, v202
	ds_read_b128 v[252:255], v252
	v_add_u32_e32 v202, v218, v202
	s_waitcnt lgkmcnt(3)
	v_mfma_f32_32x32x16_bf16 v[96:111], v[236:239], v[16:19], 0
	v_add_u32_e32 v228, v23, v220
	ds_read_b128 v[228:231], v228
	s_waitcnt lgkmcnt(3)
	v_mfma_f32_32x32x16_bf16 v[80:95], v[240:243], v[16:19], 0
	v_add_u32_e32 v232, v28, v220
	ds_read_b128 v[232:235], v232
	s_waitcnt lgkmcnt(3)
	v_mfma_f32_32x32x16_bf16 v[96:111], v[244:247], v[172:175], v[96:111]
	v_add_u32_e32 v236, v23, v219
	ds_read_b128 v[236:239], v236
	s_waitcnt lgkmcnt(3)
	v_mfma_f32_32x32x16_bf16 v[80:95], v[252:255], v[172:175], v[80:95]
	v_add_u32_e32 v240, v28, v219
	ds_read_b128 v[240:243], v240
	s_waitcnt lgkmcnt(3)
	v_mfma_f32_32x32x16_bf16 v[96:111], v[228:231], v[168:171], v[96:111]
	v_add_u32_e32 v244, v23, v217
	ds_read_b128 v[244:247], v244
	s_waitcnt lgkmcnt(3)
	v_mfma_f32_32x32x16_bf16 v[80:95], v[232:235], v[168:171], v[80:95]
	v_add_u32_e32 v252, v28, v217
	ds_read_b128 v[252:255], v252
	s_waitcnt lgkmcnt(3)
	v_mfma_f32_32x32x16_bf16 v[96:111], v[236:239], v[112:115], v[96:111]
	v_add_u32_e32 v228, v23, v216
	ds_read_b128 v[228:231], v228
	s_waitcnt lgkmcnt(3)
	v_mfma_f32_32x32x16_bf16 v[80:95], v[240:243], v[112:115], v[80:95]
	v_add_u32_e32 v232, v28, v216
	ds_read_b128 v[232:235], v232
	s_waitcnt lgkmcnt(3)
	v_mfma_f32_32x32x16_bf16 v[96:111], v[244:247], v[116:119], v[96:111]
	v_add_u32_e32 v236, v23, v215
	ds_read_b128 v[236:239], v236
	s_waitcnt lgkmcnt(3)
	v_mfma_f32_32x32x16_bf16 v[80:95], v[252:255], v[116:119], v[80:95]
	v_add_u32_e32 v240, v28, v215
	ds_read_b128 v[240:243], v240
	s_waitcnt lgkmcnt(3)
	v_mfma_f32_32x32x16_bf16 v[96:111], v[228:231], v[122:125], v[96:111]
	v_add_u32_e32 v244, v23, v214
	ds_read_b128 v[244:247], v244
	s_waitcnt lgkmcnt(3)
	v_mfma_f32_32x32x16_bf16 v[80:95], v[232:235], v[122:125], v[80:95]
	v_add_u32_e32 v252, v28, v214
	ds_read_b128 v[252:255], v252
	s_waitcnt lgkmcnt(3)
	v_mfma_f32_32x32x16_bf16 v[96:111], v[236:239], v[164:167], v[96:111]
	v_add_u32_e32 v228, v23, v210
	ds_read_b128 v[228:231], v228
	s_waitcnt lgkmcnt(3)
	v_mfma_f32_32x32x16_bf16 v[80:95], v[240:243], v[164:167], v[80:95]
	v_add_u32_e32 v232, v28, v210
	ds_read_b128 v[232:235], v232
	s_waitcnt lgkmcnt(3)
	v_mfma_f32_32x32x16_bf16 v[96:111], v[244:247], v[160:163], v[96:111]
	v_add_u32_e32 v236, v23, v211
	ds_read_b128 v[236:239], v236
	s_waitcnt lgkmcnt(3)
	v_mfma_f32_32x32x16_bf16 v[80:95], v[252:255], v[160:163], v[80:95]
	v_add_u32_e32 v240, v28, v211
	ds_read_b128 v[240:243], v240
	s_waitcnt lgkmcnt(3)
	v_mfma_f32_32x32x16_bf16 v[96:111], v[228:231], v[156:159], v[96:111]
	v_add_u32_e32 v244, v23, v212
	ds_read_b128 v[244:247], v244
	s_waitcnt lgkmcnt(3)
	v_mfma_f32_32x32x16_bf16 v[80:95], v[232:235], v[156:159], v[80:95]
	v_add_u32_e32 v252, v28, v212
	ds_read_b128 v[252:255], v252
	s_waitcnt lgkmcnt(3)
	v_mfma_f32_32x32x16_bf16 v[96:111], v[236:239], v[152:155], v[96:111]
	v_add_u32_e32 v228, v23, v213
	ds_read_b128 v[228:231], v228
	s_waitcnt lgkmcnt(3)
	v_mfma_f32_32x32x16_bf16 v[80:95], v[240:243], v[152:155], v[80:95]
	ds_read_b128 v[232:235], v29
	v_add_u32_e32 v29, v23, v206
	s_waitcnt lgkmcnt(3)
	v_mfma_f32_32x32x16_bf16 v[96:111], v[244:247], v[148:151], v[96:111]
	ds_read_b128 v[236:239], v29
	v_add_u32_e32 v29, v28, v206
	s_waitcnt lgkmcnt(3)
	v_mfma_f32_32x32x16_bf16 v[80:95], v[252:255], v[148:151], v[80:95]
	ds_read_b128 v[240:243], v29
	v_add_u32_e32 v29, v23, v207
	s_waitcnt lgkmcnt(3)
	v_mfma_f32_32x32x16_bf16 v[96:111], v[228:231], v[128:131], v[96:111]
	ds_read_b128 v[244:247], v29
	v_add_u32_e32 v29, v28, v207
	s_waitcnt lgkmcnt(3)
	v_mfma_f32_32x32x16_bf16 v[80:95], v[232:235], v[128:131], v[80:95]
	ds_read_b128 v[252:255], v29
	v_add_u32_e32 v29, v23, v208
	v_add_u32_e32 v23, v23, v209
	s_waitcnt lgkmcnt(3)
	v_mfma_f32_32x32x16_bf16 v[96:111], v[236:239], v[144:147], v[96:111]
	ds_read_b128 v[228:231], v29
	v_add_u32_e32 v29, v28, v208
	s_waitcnt lgkmcnt(3)
	v_mfma_f32_32x32x16_bf16 v[80:95], v[240:243], v[144:147], v[80:95]
	ds_read_b128 v[232:235], v29
	s_waitcnt lgkmcnt(3)
	v_mfma_f32_32x32x16_bf16 v[96:111], v[244:247], v[140:143], v[96:111]
	ds_read_b128 v[236:239], v23
	v_add_u32_e32 v23, v28, v209
	s_waitcnt lgkmcnt(3)
	v_mfma_f32_32x32x16_bf16 v[80:95], v[252:255], v[140:143], v[80:95]
	ds_read_b128 v[240:243], v23
	s_waitcnt lgkmcnt(3)
	v_mfma_f32_32x32x16_bf16 v[96:111], v[228:231], v[132:135], v[96:111]
	s_waitcnt lgkmcnt(2)
	v_mfma_f32_32x32x16_bf16 v[80:95], v[232:235], v[132:135], v[80:95]
	s_waitcnt lgkmcnt(1)
	v_mfma_f32_32x32x16_bf16 v[96:111], v[236:239], v[136:139], v[96:111]
	s_waitcnt lgkmcnt(0)
	v_mfma_f32_32x32x16_bf16 v[80:95], v[240:243], v[136:139], v[80:95]
	ds_read_b128 v[24:27], v20
	v_add_u32_e32 v20, v218, v21
	ds_read_b128 v[20:23], v20
	s_waitcnt lgkmcnt(1)
	v_mfma_f32_32x32x16_bf16 v[32:47], v[24:27], v[16:19], 0
	v_mfma_f32_32x32x16_bf16 v[32:47], v[222:225], v[172:175], v[32:47]
	ds_read_b128 v[222:225], v202
	v_add_u32_e32 v202, v221, v220
	ds_read_b128 v[226:229], v202
	s_waitcnt lgkmcnt(2)
	v_mfma_f32_32x32x16_bf16 v[16:31], v[20:23], v[16:19], 0
	s_waitcnt lgkmcnt(1)
	v_mfma_f32_32x32x16_bf16 v[16:31], v[222:225], v[172:175], v[16:31]
	v_lshl_add_u64 v[174:175], v[126:127], 0, v[180:181]
	v_add_u32_e32 v126, v218, v220
	ds_read_b128 v[222:225], v126
	v_mov_b32_e32 v126, v177
	v_add_u32_e32 v177, v221, v219
	v_mov_b32_e32 v127, v178
	v_lshl_add_u64 v[172:173], v[188:189], 0, v[184:185]
	s_waitcnt lgkmcnt(1)
	v_mfma_f32_32x32x16_bf16 v[32:47], v[226:229], v[168:171], v[32:47]
	ds_read_b128 v[226:229], v177
	v_mov_b32_e32 v177, v179
	v_add_f32_e64 v126, v126, v176
	v_add_f32_e64 v127, v127, v177
	v_lshl_add_u64 v[188:189], v[120:121], 0, v[186:187]
	v_add_f32_e32 v126, v126, v127
	v_add_u32_e32 v127, v218, v219
	ds_read_b128 v[176:179], v127
	s_waitcnt lgkmcnt(2)
	v_mfma_f32_32x32x16_bf16 v[16:31], v[222:225], v[168:171], v[16:31]
	v_fmamk_f32 v126, v126, 0x3b800000, v198
	v_rsq_f32_e32 v126, v126
	v_lshlrev_b32_e32 v120, 8, v200
	v_mov_b32_e32 v121, v181
	v_lshl_add_u64 v[170:171], s[4:5], 0, v[120:121]
	v_mul_f32_e32 v168, 0x3dd53b94, v126
	v_lshlrev_b32_e32 v169, 3, v204
	v_add_u32_e32 v120, v221, v217
	ds_read_b128 v[222:225], v120
	v_pk_mul_f32 v[64:65], v[168:169], v[64:65] op_sel_hi:[0,1]
	s_waitcnt lgkmcnt(2)
	v_mfma_f32_32x32x16_bf16 v[32:47], v[226:229], v[112:115], v[32:47]
	v_mul_f32_e64 v66, v168, v66
	v_mul_f32_e64 v67, v168, v67
	v_mul_f32_e64 v68, v168, v68
	v_mul_f32_e64 v69, v168, v69
	v_mul_f32_e64 v70, v168, v70
	v_mul_f32_e64 v71, v168, v71
	v_pk_mul_f32 v[48:49], v[168:169], v[48:49] op_sel_hi:[0,1]
	v_cvt_pk_bf16_f32 v120, v48, v49
	v_add_u32_e32 v48, v221, v215
	v_pk_mul_f32 v[78:79], v[168:169], v[78:79] op_sel_hi:[0,1]
	s_waitcnt lgkmcnt(1)
	v_mfma_f32_32x32x16_bf16 v[16:31], v[176:179], v[112:115], v[16:31]
	v_cvt_pk_bf16_f32 v112, v64, v65
	v_add_u32_e32 v64, v218, v217
	v_cvt_pk_bf16_f32 v113, v66, v67
	ds_read_b128 v[64:67], v64
	v_cvt_pk_bf16_f32 v114, v68, v69
	v_add_u32_e32 v68, v221, v216
	v_cvt_pk_bf16_f32 v115, v70, v71
	ds_read_b128 v[68:71], v68
	s_waitcnt lgkmcnt(2)
	v_mfma_f32_32x32x16_bf16 v[32:47], v[222:225], v[116:119], v[32:47]
	v_mul_f32_e64 v52, v168, v52
	v_mul_f32_e64 v53, v168, v53
	v_mul_f32_e64 v54, v168, v54
	v_mul_f32_e64 v55, v168, v55
	v_mul_f32_e64 v72, v168, v72
	v_mul_f32_e64 v73, v168, v73
	v_pk_mul_f32 v[60:61], v[168:169], v[60:61] op_sel_hi:[0,1]
	v_pk_mul_f32 v[62:63], v[168:169], v[62:63] op_sel_hi:[0,1]
	v_cvt_pk_bf16_f32 v126, v60, v61
	v_cvt_pk_bf16_f32 v127, v62, v63
	s_waitcnt lgkmcnt(1)
	v_mfma_f32_32x32x16_bf16 v[16:31], v[64:67], v[116:119], v[16:31]
	v_mul_f32_e64 v64, v168, v74
	v_mul_f32_e64 v65, v168, v75
	v_cvt_pk_bf16_f32 v117, v64, v65
	v_add_u32_e32 v64, v218, v216
	ds_read_b128 v[64:67], v64
	v_cvt_pk_bf16_f32 v119, v78, v79
	v_pk_mul_f32 v[78:79], v[168:169], v[88:89] op_sel_hi:[0,1]
	v_cvt_pk_bf16_f32 v116, v72, v73
	s_waitcnt lgkmcnt(1)
	v_mfma_f32_32x32x16_bf16 v[32:47], v[68:71], v[122:125], v[32:47]
	v_mul_f32_e64 v68, v168, v50
	v_mul_f32_e64 v69, v168, v51
	ds_read_b128 v[48:51], v48
	v_mul_f32_e64 v70, v168, v86
	v_mul_f32_e64 v71, v168, v87
	v_add_u32_e32 v86, v218, v213
	ds_read_b128 v[86:89], v86
	v_pk_mul_f32 v[60:61], v[168:169], v[100:101] op_sel_hi:[0,1]
	v_pk_mul_f32 v[62:63], v[168:169], v[102:103] op_sel_hi:[0,1]
	s_waitcnt lgkmcnt(2)
	v_mfma_f32_32x32x16_bf16 v[16:31], v[64:67], v[122:125], v[16:31]
	v_cvt_pk_bf16_f32 v122, v52, v53
	v_add_u32_e32 v52, v218, v215
	v_cvt_pk_bf16_f32 v123, v54, v55
	ds_read_b128 v[52:55], v52
	v_mul_f32_e64 v64, v168, v98
	v_mul_f32_e64 v65, v168, v99
	v_cvt_pk_bf16_f32 v98, v60, v61
	v_cvt_pk_bf16_f32 v99, v62, v63
	s_waitcnt lgkmcnt(2)
	v_mfma_f32_32x32x16_bf16 v[32:47], v[48:51], v[164:167], v[32:47]
	v_mul_f32_e64 v48, v168, v56
	v_mul_f32_e64 v49, v168, v57
	v_mul_f32_e64 v50, v168, v58
	v_mul_f32_e64 v51, v168, v59
	v_cvt_pk_bf16_f32 v124, v48, v49
	v_add_u32_e32 v48, v221, v214
	v_cvt_pk_bf16_f32 v125, v50, v51
	ds_read_b128 v[48:51], v48
	v_and_b32_e32 v58, 32, v205
	s_waitcnt lgkmcnt(1)
	v_mfma_f32_32x32x16_bf16 v[16:31], v[52:55], v[164:167], v[16:31]
	v_add_u32_e32 v52, v218, v214
	ds_read_b128 v[52:55], v52
	v_mov_b32_e32 v59, v181
	v_lshl_add_u64 v[72:73], v[170:171], 0, v[58:59]
	v_mul_f32_e64 v56, v168, v96
	v_mul_f32_e64 v57, v168, v97
	v_cvt_pk_bf16_f32 v96, v56, v57
	v_add_u32_e32 v56, v221, v210
	s_waitcnt lgkmcnt(1)
	v_mfma_f32_32x32x16_bf16 v[32:47], v[48:51], v[160:163], v[32:47]
	global_load_dwordx4 v[48:51], v[72:73], off offset:16
	ds_read_b128 v[56:59], v56
	v_cvt_pk_bf16_f32 v97, v64, v65
	v_mul_f32_e64 v64, v168, v106
	v_mul_f32_e64 v65, v168, v107
	v_cvt_pk_bf16_f32 v101, v64, v65
	v_cvt_pk_bf16_f32 v121, v68, v69
	v_pk_mul_f32 v[68:69], v[168:169], v[108:109] op_sel_hi:[0,1]
	s_waitcnt lgkmcnt(1)
	v_mfma_f32_32x32x16_bf16 v[16:31], v[52:55], v[160:163], v[16:31]
	v_add_u32_e32 v52, v221, v211
	ds_read_b128 v[60:63], v52
	global_load_dwordx4 v[52:55], v[72:73], off
	v_cvt_pk_bf16_f32 v102, v68, v69
	v_mul_f32_e64 v68, v168, v84
	v_mul_f32_e64 v69, v168, v85
	v_cvt_pk_bf16_f32 v106, v68, v69
	v_add_u32_e32 v68, v221, v207
	s_waitcnt lgkmcnt(1)
	v_mfma_f32_32x32x16_bf16 v[32:47], v[56:59], v[156:159], v[32:47]
	v_mul_f32_e64 v58, v168, v104
	v_mul_f32_e64 v59, v168, v105
	v_cvt_pk_bf16_f32 v100, v58, v59
	v_add_u32_e32 v58, v221, v212
	ds_read_b128 v[64:67], v58
	v_pk_mul_f32 v[56:57], v[168:169], v[110:111] op_sel_hi:[0,1]
	v_cvt_pk_bf16_f32 v103, v56, v57
	v_add_u32_e32 v56, v221, v213
	s_waitcnt lgkmcnt(1)
	v_mfma_f32_32x32x16_bf16 v[32:47], v[60:63], v[152:155], v[32:47]
	ds_read_b128 v[60:63], v56
	v_cvt_pk_bf16_f32 v107, v70, v71
	ds_read_b128 v[68:71], v68
	v_mul_f32_e64 v76, v168, v76
	v_mul_f32_e64 v77, v168, v77
	v_cvt_pk_bf16_f32 v118, v76, v77
	v_pk_mul_f32 v[74:75], v[168:169], v[92:93] op_sel_hi:[0,1]
	v_pk_mul_f32 v[76:77], v[168:169], v[94:95] op_sel_hi:[0,1]
	s_waitcnt lgkmcnt(2)
	v_mfma_f32_32x32x16_bf16 v[32:47], v[64:67], v[148:151], v[32:47]
	v_mul_f32_e64 v64, v168, v80
	v_mul_f32_e64 v65, v168, v81
	v_mul_f32_e64 v66, v168, v82
	v_mul_f32_e64 v67, v168, v83
	v_cvt_pk_bf16_f32 v104, v64, v65
	v_add_u32_e32 v64, v221, v206
	v_cvt_pk_bf16_f32 v105, v66, v67
	ds_read_b128 v[64:67], v64
	global_load_dwordx4 v[56:59], v[72:73], off offset:80
	s_waitcnt lgkmcnt(2)
	v_mfma_f32_32x32x16_bf16 v[32:47], v[60:63], v[128:131], v[32:47]
	v_cvt_pk_bf16_f32 v110, v74, v75
	v_cvt_pk_bf16_f32 v111, v76, v77
	v_cvt_pk_bf16_f32 v108, v78, v79
	global_load_dwordx4 v[60:63], v[72:73], off offset:64
	global_load_dwordx4 v[164:167], v[72:73], off offset:128
	v_add_u32_e32 v94, v218, v207
	s_movk_i32 s4, 0x180
	s_waitcnt lgkmcnt(0)
	v_mfma_f32_32x32x16_bf16 v[32:47], v[64:67], v[144:147], v[32:47]
	v_mul_f32_e64 v64, v168, v90
	v_mul_f32_e64 v65, v168, v91
	v_cvt_pk_bf16_f32 v109, v64, v65
	v_add_u32_e32 v64, v221, v208
	ds_read_b128 v[64:67], v64
	v_add_u32_e32 v90, v218, v206
	ds_read_b128 v[90:93], v90
	v_or_b32_e32 v202, s6, v203
	v_mfma_f32_32x32x16_bf16 v[32:47], v[68:71], v[140:143], v[32:47]
	v_add_u32_e32 v68, v218, v210
	ds_read_b128 v[74:77], v68
	v_add_u32_e32 v68, v218, v211
	v_add_u32_e32 v69, v221, v209
	ds_read_b128 v[78:81], v68
	ds_read_b128 v[82:85], v69
	v_add_u32_e32 v68, v218, v212
	s_waitcnt lgkmcnt(4)
	v_mfma_f32_32x32x16_bf16 v[32:47], v[64:67], v[132:135], v[32:47]
	global_load_dwordx4 v[64:67], v[72:73], off offset:144
	ds_read_b128 v[68:71], v68
	s_sub_i32 s5, 0, s25
	s_waitcnt lgkmcnt(1)
	v_mfma_f32_32x32x16_bf16 v[32:47], v[82:85], v[136:139], v[32:47]
	ds_read_b128 v[82:85], v94
	v_add_u32_e32 v94, v218, v208
	ds_read_b128 v[160:163], v94
	v_add_u32_e32 v94, v218, v209
	ds_read_b128 v[176:179], v94
	s_nop 6
	v_mul_f32_e32 v36, v168, v36
	v_mfma_f32_32x32x16_bf16 v[16:31], v[74:77], v[156:159], v[16:31]
	v_mul_f32_e32 v74, v168, v37
	s_waitcnt vmcnt(5)
	v_pk_mul_f32 v[74:75], v[74:75], v[48:49] op_sel:[0,1] op_sel_hi:[0,0]
	v_pk_fma_f32 v[76:77], v[36:37], v[48:49], v[74:75] neg_lo:[0,0,1] neg_hi:[0,0,1]
	v_pk_fma_f32 v[48:49], v[36:37], v[48:49], v[74:75] op_sel_hi:[0,1,1]
	v_mul_f32_e32 v36, v168, v39
	v_mul_f32_e32 v48, v168, v38
	v_pk_mul_f32 v[74:75], v[36:37], v[50:51] op_sel:[0,1] op_sel_hi:[0,0]
	global_load_dwordx4 v[36:39], v[72:73], off offset:208
	v_mfma_f32_32x32x16_bf16 v[16:31], v[78:81], v[152:155], v[16:31]
	v_fma_f32 v78, v48, v50, -v74
	v_fma_f32 v79, v49, v51, -v75
	v_fma_f32 v50, v48, v50, v74
	v_fma_f32 v51, v48, v51, v75
	v_mul_f32_e32 v48, v168, v33
	v_mul_f32_e32 v32, v168, v32
	s_waitcnt vmcnt(5)
	v_pk_mul_f32 v[74:75], v[48:49], v[52:53] op_sel:[0,1] op_sel_hi:[0,0]
	v_pk_fma_f32 v[80:81], v[32:33], v[52:53], v[74:75] neg_lo:[0,0,1] neg_hi:[0,0,1]
	v_pk_fma_f32 v[52:53], v[32:33], v[52:53], v[74:75] op_sel_hi:[0,1,1]
	v_mul_f32_e32 v48, v168, v34
	v_mul_f32_e32 v50, v168, v35
	global_load_dwordx4 v[32:35], v[72:73], off offset:192
	s_waitcnt lgkmcnt(3)
	v_mfma_f32_32x32x16_bf16 v[16:31], v[68:71], v[148:151], v[16:31]
	v_mul_f32_e64 v68, v50, v55
	v_mul_f32_e64 v69, v50, v54
	v_fma_f32 v70, v48, v54, -v68
	v_fma_f32 v71, v49, v55, -v69
	v_fma_f32 v54, v48, v54, v68
	v_fma_f32 v55, v48, v55, v69
	v_mul_f32_e32 v48, v168, v45
	v_mul_f32_e32 v44, v168, v44
	v_mul_f32_e32 v40, v168, v40
	v_mov_b32_e32 v158, 0
	v_mfma_f32_32x32x16_bf16 v[16:31], v[86:89], v[128:131], v[16:31]
	v_cvt_pk_bf16_f32 v130, v76, v49
	v_cvt_pk_bf16_f32 v131, v78, v51
	v_cvt_pk_bf16_f32 v128, v80, v53
	v_cvt_pk_bf16_f32 v129, v70, v55
	s_cmp_eq_u32 s99, 0
	s_cselect_b32 s101, 1, 0
	s_cselect_b32 s99, 0, 2
	v_mov_b32_e32 v157, 0xf149f2ca
	s_cbranch_scc0 .Linit_done
	v_mov_b32_e32 v157, 0
